# v89 + attention item loop top waits only for the claim atomic (vmcnt(4), younger output stores stay in flight); phase F second-half residual loads waited with vmcnt(2)
# speedup vs baseline: 1.0014x; 1.0014x over previous
.LBB0_3603:
	s_and_saveexec_b64 s[4:5], s[74:75]
	s_cbranch_execz .LBB0_3607
	s_mov_b64 s[8:9], exec
	v_mbcnt_lo_u32_b32 v0, s8, 0
	v_mbcnt_hi_u32_b32 v0, s9, v0
	v_cmp_eq_u32_e32 vcc, 0, v0
	s_and_saveexec_b64 s[6:7], vcc
	s_cbranch_execz .LBB0_3606
	s_cmp_eq_u32 s32, 0
	s_cbranch_scc1 .Lqe_demand
	s_waitcnt vmcnt(4)
	v_mov_b32_e32 v2, v190
	s_mov_b32 s32, 0
	s_branch .LBB0_3606
.Lqe_demand:
	s_bcnt1_i32_b64 s0, s[8:9]
	v_mov_b32_e32 v2, s0
	global_atomic_add v2, v1, v2, s[50:51] sc0
	s_waitcnt vmcnt(0)
.LBB0_3606:
	s_or_b64 exec, exec, s[6:7]
	v_readfirstlane_b32 s0, v2
	v_mov_b32_e32 v2, s59
	s_nop 0
	v_add_u32_e32 v0, s0, v0
	ds_write_b32 v2, v0

.LBB0_3967:
	s_or_b64 exec, exec, s[22:23]
	v_add_u32_e32 v42, 0x80, v28
	v_ashrrev_i32_e32 v43, 31, v42
	v_add_u32_e32 v38, 0x90, v28
	v_lshlrev_b64 v[52:53], 12, v[42:43]
	v_ashrrev_i32_e32 v39, 31, v38
	v_add_u32_e32 v34, 0xa0, v28
	s_waitcnt lgkmcnt(0)
	v_lshl_add_u64 v[2:3], v[30:31], 0, v[52:53]
	v_lshlrev_b64 v[40:41], 12, v[38:39]
	v_ashrrev_i32_e32 v35, 31, v34
	v_add_u32_e32 v28, 0xb0, v28
	v_lshl_add_u64 v[2:3], v[30:31], 0, v[40:41]
	v_lshlrev_b64 v[36:37], 12, v[34:35]
	v_ashrrev_i32_e32 v29, 31, v28
	v_lshl_add_u64 v[2:3], v[30:31], 0, v[36:37]
	v_lshlrev_b64 v[32:33], 12, v[28:29]
	v_lshl_add_u64 v[2:3], v[30:31], 0, v[32:33]
	s_nop 0
	v_lshl_add_u64 v[52:53], s[8:9], 0, v[52:53]
	v_lshl_add_u64 v[52:53], v[26:27], 1, v[52:53]
	s_waitcnt vmcnt(2)
	v_mov_b64_e32 v[44:45], v[178:179]
	v_mov_b64_e32 v[46:47], v[180:181]
	v_mov_b64_e32 v[48:49], v[182:183]
	v_mov_b64_e32 v[50:51], v[184:185]
	v_mov_b64_e32 v[22:23], v[162:163]
	v_mov_b64_e32 v[24:25], v[164:165]
	v_mov_b64_e32 v[18:19], v[166:167]
	v_mov_b64_e32 v[20:21], v[168:169]
	v_mov_b64_e32 v[14:15], v[170:171]
	v_mov_b64_e32 v[16:17], v[172:173]
	v_mov_b64_e32 v[10:11], v[174:175]
	v_mov_b64_e32 v[12:13], v[176:177]
	v_mov_b64_e32 v[6:7], v[146:147]
	v_mov_b64_e32 v[8:9], v[148:149]
	v_mov_b64_e32 v[2:3], v[150:151]
	v_mov_b64_e32 v[4:5], v[152:153]
	s_nop 0
	v_and_b32_e32 v31, 0xffff0000, v44
	v_lshlrev_b32_e32 v30, 16, v44
	v_and_b32_e32 v55, 0xffff0000, v45
	v_lshlrev_b32_e32 v54, 16, v45
	v_pk_fma_f32 v[30:31], v[126:127], s[78:79], v[30:31] op_sel_hi:[1,0,1]
	v_and_b32_e32 v45, 0xffff0000, v46
	v_lshlrev_b32_e32 v44, 16, v46
	v_pk_fma_f32 v[54:55], v[128:129], s[78:79], v[54:55] op_sel_hi:[1,0,1]
	v_and_b32_e32 v57, 0xffff0000, v47
	v_lshlrev_b32_e32 v56, 16, v47
	v_pk_fma_f32 v[58:59], v[122:123], s[78:79], v[44:45] op_sel_hi:[1,0,1]
	v_cvt_pk_bf16_f32 v44, v30, v31
	v_mul_f32_e32 v31, v31, v31
	v_pk_fma_f32 v[56:57], v[124:125], s[78:79], v[56:57] op_sel_hi:[1,0,1]
	v_fmac_f32_e32 v31, v30, v30
	v_mul_f32_e32 v30, v55, v55
	v_cvt_pk_bf16_f32 v45, v54, v55
	v_cvt_pk_bf16_f32 v46, v58, v59
	v_cvt_pk_bf16_f32 v47, v56, v57
	v_fmac_f32_e32 v30, v54, v54
	global_store_dwordx4 v[52:53], v[44:47], off
	v_add_f32_e32 v30, v31, v30
	v_mul_f32_e32 v31, v59, v59
	v_mul_f32_e32 v44, v57, v57
	v_fmac_f32_e32 v31, v58, v58
	v_fmac_f32_e32 v44, v56, v56
	v_add_f32_e32 v31, v31, v44
	v_add_f32_e32 v56, v30, v31
	v_and_b32_e32 v31, 0xffff0000, v48
	v_lshlrev_b32_e32 v30, 16, v48
	v_and_b32_e32 v45, 0xffff0000, v49
	v_lshlrev_b32_e32 v44, 16, v49
	v_pk_fma_f32 v[48:49], v[120:121], s[78:79], v[44:45] op_sel_hi:[1,0,1]
	v_pk_fma_f32 v[30:31], v[118:119], s[78:79], v[30:31] op_sel_hi:[1,0,1]
	v_and_b32_e32 v45, 0xffff0000, v50
	v_lshlrev_b32_e32 v44, 16, v50
	v_and_b32_e32 v47, 0xffff0000, v51
	v_lshlrev_b32_e32 v46, 16, v51
	v_pk_fma_f32 v[54:55], v[114:115], s[78:79], v[44:45] op_sel_hi:[1,0,1]
	v_cvt_pk_bf16_f32 v44, v30, v31
	v_mul_f32_e32 v31, v31, v31
	v_pk_fma_f32 v[50:51], v[116:117], s[78:79], v[46:47] op_sel_hi:[1,0,1]
	v_fmac_f32_e32 v31, v30, v30
	v_mul_f32_e32 v30, v49, v49
	v_cvt_pk_bf16_f32 v45, v48, v49
	v_cvt_pk_bf16_f32 v46, v54, v55
	v_cvt_pk_bf16_f32 v47, v50, v51
	v_fmac_f32_e32 v30, v48, v48
	global_store_dwordx4 v[52:53], v[44:47], off offset:256
	v_add_f32_e32 v30, v31, v30
	v_mul_f32_e32 v31, v55, v55
	v_mul_f32_e32 v44, v51, v51
	v_fmac_f32_e32 v31, v54, v54
	v_fmac_f32_e32 v44, v50, v50
	v_add_f32_e32 v31, v31, v44
	v_add_f32_e32 v30, v30, v31
	v_add_f32_e32 v30, v56, v30
	ds_bpermute_b32 v31, v249, v30
	s_waitcnt lgkmcnt(0)
	v_add_f32_e32 v30, v30, v31
	ds_bpermute_b32 v31, v250, v30
	s_and_saveexec_b64 s[22:23], vcc
	s_cbranch_execz .LBB0_3969
	v_lshlrev_b64 v[42:43], 7, v[42:43]
	v_lshl_add_u64 v[42:43], s[10:11], 0, v[42:43]
	v_lshl_add_u64 v[42:43], s[20:21], 2, v[42:43]
	s_lshl_b32 s92, s42, 2
	v_lshl_add_u64 v[42:43], v[42:43], 0, s[92:93]
	s_waitcnt lgkmcnt(0)
	v_add_f32_e32 v30, v30, v31
	global_store_dword v[42:43], v30, off
